# T1-T3: norm/adaLN table builds de-serialised (combine: next-layer norm1 tables + g2 gate table; norm2 stage tables): all table loads issued together with one wait instead of 8-23 serial load/wait step
# speedup vs baseline: 1.0111x; 1.0087x over previous
.LBB0_1125:
	s_or_b64 exec, exec, s[0:1]
	s_mov_b64 s[0:1], 0
	v_readlane_b32 s4, v253, 0
	s_waitcnt lgkmcnt(0)
	v_mov_b32_e32 v0, v169
	s_barrier
	v_readlane_b32 s5, v253, 1
	v_readlane_b32 s16, v253, 12
	v_readlane_b32 s6, v253, 2
	v_readlane_b32 s17, v253, 13
	s_add_u32 s5, s16, s0
	v_mbcnt_lo_u32_b32 v0, -1, v0
	v_readlane_b32 s9, v253, 5
	s_addc_u32 s6, s17, s1
	v_mbcnt_hi_u32_b32 v0, -1, v0
	v_readlane_b32 s10, v253, 6
	s_add_u32 s9, s76, s0
	v_or_b32_e32 v2, s75, v0
	v_readlane_b32 s8, v253, 4
	s_addc_u32 s10, s77, s1
	s_ashr_i32 s83, s82, 31
	v_readfirstlane_b32 s2, v2
	s_ashr_i32 s8, s2, 6
	s_lshl_b64 s[2:3], s[82:83], 13
	s_add_u32 s2, s5, s2
	s_addc_u32 s3, s6, s3
	v_readlane_b32 s7, v253, 3
	s_add_u32 s6, s9, 0x100000
	v_readlane_b32 s13, v253, 9
	s_addc_u32 s7, s10, 0
	s_lshl_b32 s5, s82, 2
	s_mov_b32 s13, 0xc000
	v_readlane_b32 s12, v253, 8
	s_mov_b32 s12, 0x8000
	v_readlane_b32 s11, v253, 7
	s_movk_i32 s11, 0x6000
	s_mov_b32 s4, s74
	v_lshlrev_b32_e32 v4, 2, v2
	v_add_u32_e32 v6, 0x1000, v4
	v_add_u32_e32 v7, 0x6000, v4
	v_add_u32_e32 v8, 0x7000, v4
	v_add_u32_e32 v9, 0x8000, v4
	v_add_u32_e32 v10, 0x9000, v4
	s_mul_i32 s20, s5, 0xc000
	s_add_u32 s20, s6, s20
	s_addc_u32 s21, s7, 0
	s_add_u32 s22, s20, 0xc000
	s_addc_u32 s23, s21, 0
	s_add_u32 s24, s20, 0x18000
	s_addc_u32 s25, s21, 0
	s_add_u32 s26, s20, 0x24000
	s_addc_u32 s27, s21, 0
	global_load_dword v12, v4, s[2:3]
	global_load_dword v13, v4, s[2:3] offset:2048
	global_load_dword v14, v6, s[2:3]
	global_load_dword v15, v6, s[2:3] offset:2048
	global_load_dword v16, v9, s[20:21]
	global_load_dword v32, v7, s[20:21]
	global_load_dword v17, v9, s[20:21] offset:2048
	global_load_dword v33, v7, s[20:21] offset:2048
	global_load_dword v18, v10, s[20:21]
	global_load_dword v34, v8, s[20:21]
	global_load_dword v19, v10, s[20:21] offset:2048
	global_load_dword v35, v8, s[20:21] offset:2048
	global_load_dword v20, v9, s[22:23]
	global_load_dword v36, v7, s[22:23]
	global_load_dword v21, v9, s[22:23] offset:2048
	global_load_dword v37, v7, s[22:23] offset:2048
	global_load_dword v22, v10, s[22:23]
	global_load_dword v38, v8, s[22:23]
	global_load_dword v23, v10, s[22:23] offset:2048
	global_load_dword v39, v8, s[22:23] offset:2048
	global_load_dword v24, v9, s[24:25]
	global_load_dword v40, v7, s[24:25]
	global_load_dword v25, v9, s[24:25] offset:2048
	global_load_dword v41, v7, s[24:25] offset:2048
	global_load_dword v26, v10, s[24:25]
	global_load_dword v42, v8, s[24:25]
	global_load_dword v27, v10, s[24:25] offset:2048
	global_load_dword v43, v8, s[24:25] offset:2048
	global_load_dword v28, v9, s[26:27]
	global_load_dword v44, v7, s[26:27]
	global_load_dword v29, v9, s[26:27] offset:2048
	global_load_dword v45, v7, s[26:27] offset:2048
	global_load_dword v30, v10, s[26:27]
	global_load_dword v46, v8, s[26:27]
	global_load_dword v31, v10, s[26:27] offset:2048
	global_load_dword v47, v8, s[26:27] offset:2048
	s_waitcnt vmcnt(0)
	v_add_f32_e32 v16, 1.0, v16
	v_add_f32_e32 v17, 1.0, v17
	v_add_f32_e32 v18, 1.0, v18
	v_add_f32_e32 v19, 1.0, v19
	v_add_f32_e32 v20, 1.0, v20
	v_add_f32_e32 v21, 1.0, v21
	v_add_f32_e32 v22, 1.0, v22
	v_add_f32_e32 v23, 1.0, v23
	v_add_f32_e32 v24, 1.0, v24
	v_add_f32_e32 v25, 1.0, v25
	v_add_f32_e32 v26, 1.0, v26
	v_add_f32_e32 v27, 1.0, v27
	v_add_f32_e32 v28, 1.0, v28
	v_add_f32_e32 v29, 1.0, v29
	v_add_f32_e32 v30, 1.0, v30
	v_add_f32_e32 v31, 1.0, v31
	v_mul_f32_e32 v16, v12, v16
	v_mul_f32_e32 v17, v13, v17
	v_mul_f32_e32 v18, v14, v18
	v_mul_f32_e32 v19, v15, v19
	v_mul_f32_e32 v20, v12, v20
	v_mul_f32_e32 v21, v13, v21
	v_mul_f32_e32 v22, v14, v22
	v_mul_f32_e32 v23, v15, v23
	v_mul_f32_e32 v24, v12, v24
	v_mul_f32_e32 v25, v13, v25
	v_mul_f32_e32 v26, v14, v26
	v_mul_f32_e32 v27, v15, v27
	v_mul_f32_e32 v28, v12, v28
	v_mul_f32_e32 v29, v13, v29
	v_mul_f32_e32 v30, v14, v30
	v_mul_f32_e32 v31, v15, v31
	ds_write2st64_b32 v4, v16, v17 offset1:8
	ds_write2st64_b32 v4, v32, v33 offset0:128 offset1:136
	ds_write2st64_b32 v4, v18, v19 offset0:16 offset1:24
	ds_write2st64_b32 v4, v34, v35 offset0:144 offset1:152
	ds_write2st64_b32 v4, v20, v21 offset0:32 offset1:40
	ds_write2st64_b32 v4, v36, v37 offset0:160 offset1:168
	ds_write2st64_b32 v4, v22, v23 offset0:48 offset1:56
	ds_write2st64_b32 v4, v38, v39 offset0:176 offset1:184
	ds_write2st64_b32 v4, v24, v25 offset0:64 offset1:72
	ds_write2st64_b32 v4, v40, v41 offset0:192 offset1:200
	ds_write2st64_b32 v4, v26, v27 offset0:80 offset1:88
	ds_write2st64_b32 v4, v42, v43 offset0:208 offset1:216
	ds_write2st64_b32 v4, v28, v29 offset0:96 offset1:104
	ds_write2st64_b32 v4, v44, v45 offset0:224 offset1:232
	ds_write2st64_b32 v4, v30, v31 offset0:112 offset1:120
	ds_write2st64_b32 v4, v46, v47 offset0:240 offset1:248
	s_mov_b32 s62, 0x8000
	s_mov_b32 s63, 0xc000
	v_readlane_b32 s14, v253, 10
	v_readlane_b32 s15, v253, 11
	v_readlane_b32 s18, v253, 14
	v_readlane_b32 s19, v253, 15
	v_lshl_add_u32 v3, v2, 2, 0
	s_lshl_b32 s2, s4, 3
	s_add_i32 s6, s8, s2
	s_cmpk_gt_i32 s6, 0x3fff
	s_waitcnt lgkmcnt(0)
	s_barrier
	s_cbranch_scc1 .LBB0_1130
	s_ashr_i32 s7, s6, 31
	s_lshl_b64 s[4:5], s[6:7], 12
	v_lshlrev_b32_e32 v0, 2, v2
	s_add_u32 s12, s9, s4
	v_and_b32_e32 v3, 0xfc, v0
	s_addc_u32 s13, s10, s5
	v_lshlrev_b32_e32 v168, 1, v3
	v_lshl_add_u64 v[0:1], s[12:13], 0, v[168:169]
	s_mov_b64 s[10:11], 0x4e400000
	s_mov_b32 s3, 0x4e400000
	v_lshl_add_u64 v[4:5], v[0:1], 0, s[10:11]
	v_add_co_u32_e32 v0, vcc, s3, v0
	s_add_i32 s3, s64, s8
	s_nop 0
	v_addc_co_u32_e32 v1, vcc, 0, v1, vcc
	global_load_dwordx2 v[30:31], v[4:5], off offset:512
	global_load_dwordx2 v[28:29], v[4:5], off offset:1024
	global_load_dwordx2 v[26:27], v[4:5], off offset:1536
	global_load_dwordx2 v[24:25], v[4:5], off offset:2048
	global_load_dwordx2 v[22:23], v[4:5], off offset:2560
	global_load_dwordx2 v[20:21], v[4:5], off offset:3072
	global_load_dwordx2 v[32:33], v[0:1], off
	global_load_dwordx2 v[18:19], v[4:5], off offset:3584
	v_and_b32_e32 v0, 64, v199
	v_xor_b32_e32 v1, 1, v199
	v_add_u32_e32 v0, 64, v0
	v_xor_b32_e32 v4, 2, v199
	v_cmp_lt_i32_e32 vcc, v1, v0
	s_add_i32 s2, s3, s2
	v_xor_b32_e32 v5, 4, v199
	v_cndmask_b32_e32 v1, v199, v1, vcc
	v_cmp_lt_i32_e32 vcc, v4, v0
	s_ashr_i32 s3, s2, 31
	v_xor_b32_e32 v6, 8, v199
	v_cndmask_b32_e32 v4, v199, v4, vcc
	v_cmp_lt_i32_e32 vcc, v5, v0
	s_lshl_b64 s[2:3], s[2:3], 12
	v_xor_b32_e32 v7, 16, v199
	v_cndmask_b32_e32 v5, v199, v5, vcc
	v_cmp_lt_i32_e32 vcc, v6, v0
	s_add_u32 s2, s2, 0x4e400800
	v_xor_b32_e32 v8, 32, v199
	v_cndmask_b32_e32 v6, v199, v6, vcc
	v_cmp_lt_i32_e32 vcc, v7, v0
	s_addc_u32 s3, s3, 0
	v_and_b32_e32 v2, 63, v2
	v_cndmask_b32_e32 v7, v199, v7, vcc
	v_cmp_lt_i32_e32 vcc, v8, v0
	s_add_u32 s0, s76, s0
	v_lshlrev_b32_e32 v168, 3, v2
	v_cndmask_b32_e32 v0, v199, v8, vcc
	s_addc_u32 s1, s77, s1
	v_lshlrev_b32_e32 v51, 2, v1
	v_lshlrev_b32_e32 v56, 2, v0
	v_lshl_add_u64 v[0:1], s[0:1], 0, v[168:169]
	s_add_u32 s0, s4, 0x35c00800
	v_lshl_add_u32 v50, v3, 2, 0
	v_lshlrev_b32_e32 v52, 2, v4
	v_lshlrev_b32_e32 v53, 2, v5
	v_lshlrev_b32_e32 v54, 2, v6
	v_lshlrev_b32_e32 v55, 2, v7
	s_addc_u32 s1, s5, 0
	s_waitcnt vmcnt(7)
	v_mov_b64_e32 v[2:3], v[30:31]
	s_waitcnt vmcnt(6)
	v_mov_b64_e32 v[4:5], v[28:29]
	s_waitcnt vmcnt(5)
	v_mov_b64_e32 v[6:7], v[26:27]
	s_waitcnt vmcnt(4)
	v_mov_b64_e32 v[10:11], v[24:25]
	s_waitcnt vmcnt(3)
	v_mov_b64_e32 v[12:13], v[22:23]
	s_waitcnt vmcnt(2)
	v_mov_b64_e32 v[14:15], v[20:21]
	s_waitcnt vmcnt(1)
	v_mov_b64_e32 v[8:9], v[32:33]
	s_waitcnt vmcnt(0)
	v_mov_b64_e32 v[16:17], v[18:19]
	s_branch .LBB0_1128

.LBB0_1580:
	s_or_b64 exec, exec, s[0:1]
	s_mov_b64 s[10:11], 0
	s_waitcnt lgkmcnt(0)
	v_mov_b32_e32 v0, v169
	s_barrier
	s_add_u32 s18, s76, s10
	v_mbcnt_lo_u32_b32 v0, -1, v0
	s_addc_u32 s19, s77, s11
	v_mbcnt_hi_u32_b32 v0, -1, v0
	s_lshl_b32 s0, s82, 2
	v_or_b32_e32 v0, s75, v0
	s_add_u32 s2, s18, 0x10a000
	s_addc_u32 s3, s19, 0
	v_ashrrev_i32_e32 v44, 11, v0
	v_add_u32_e32 v1, s0, v44
	v_mov_b64_e32 v[2:3], s[2:3]
	s_mov_b32 s1, 0xc000
	v_and_b32_e32 v1, 0x7ff, v0
	v_lshlrev_b32_e32 v168, 2, v1
	v_add_u32_e32 v1, 0x200, v0
	s_mov_b32 s14, s74
	v_ashrrev_i32_e32 v43, 11, v1
	v_add_u32_e32 v4, s0, v43
	v_and_b32_e32 v7, 0x7ff, v1
	v_lshlrev_b32_e32 v24, 2, v7
	v_mov_b32_e32 v25, v169
	v_lshl_add_u32 v28, v0, 2, 0
	v_mov_b32_e32 v23, v169
	v_add_u32_e32 v7, 0x600, v0
	v_ashrrev_i32_e32 v41, 11, v7
	v_and_b32_e32 v7, 0x7ff, v7
	v_lshlrev_b32_e32 v20, 2, v7
	v_mov_b32_e32 v21, v169
	v_add_u32_e32 v7, 0xa00, v0
	v_ashrrev_i32_e32 v39, 11, v7
	v_and_b32_e32 v7, 0x7ff, v7
	v_lshlrev_b32_e32 v18, 2, v7
	v_mov_b32_e32 v19, v169
	v_mov_b32_e32 v17, v169
	v_add_u32_e32 v7, 0xe00, v0
	v_ashrrev_i32_e32 v37, 11, v7
	v_and_b32_e32 v7, 0x7ff, v7
	v_lshlrev_b32_e32 v14, 2, v7
	v_mov_b32_e32 v15, v169
	v_add_u32_e32 v7, 0x1200, v0
	v_ashrrev_i32_e32 v35, 11, v7
	v_and_b32_e32 v7, 0x7ff, v7
	v_lshlrev_b32_e32 v12, 2, v7
	v_mov_b32_e32 v13, v169
	v_mov_b32_e32 v11, v169
	v_add_u32_e32 v7, 0x1600, v0
	v_ashrrev_i32_e32 v33, 11, v7
	v_and_b32_e32 v7, 0x7ff, v7
	v_lshlrev_b32_e32 v8, 2, v7
	v_mov_b32_e32 v9, v169
	v_mov_b32_e32 v7, v169
	v_add_u32_e32 v45, 0x1000, v28
	s_mul_i32 s20, s0, 0xc000
	s_add_u32 s20, s2, s20
	s_addc_u32 s21, s3, 0
	s_add_u32 s22, s20, 0xc000
	s_addc_u32 s23, s21, 0
	s_add_u32 s24, s20, 0x18000
	s_addc_u32 s25, s21, 0
	s_add_u32 s26, s20, 0x24000
	s_addc_u32 s27, s21, 0
	global_load_dword v46, v28, s[20:21]
	global_load_dword v47, v28, s[20:21] offset:2048
	global_load_dword v48, v45, s[20:21]
	global_load_dword v49, v45, s[20:21] offset:2048
	global_load_dword v50, v28, s[22:23]
	global_load_dword v51, v28, s[22:23] offset:2048
	global_load_dword v52, v45, s[22:23]
	global_load_dword v53, v45, s[22:23] offset:2048
	global_load_dword v54, v28, s[24:25]
	global_load_dword v55, v28, s[24:25] offset:2048
	global_load_dword v56, v45, s[24:25]
	global_load_dword v57, v45, s[24:25] offset:2048
	global_load_dword v58, v28, s[26:27]
	global_load_dword v59, v28, s[26:27] offset:2048
	global_load_dword v60, v45, s[26:27]
	global_load_dword v61, v45, s[26:27] offset:2048
	s_waitcnt vmcnt(0)
	ds_write2st64_b32 v28, v46, v47 offset1:8
	ds_write2st64_b32 v28, v48, v49 offset0:16 offset1:24
	ds_write2st64_b32 v28, v50, v51 offset0:32 offset1:40
	ds_write2st64_b32 v28, v52, v53 offset0:48 offset1:56
	ds_write2st64_b32 v28, v54, v55 offset0:64 offset1:72
	ds_write2st64_b32 v28, v56, v57 offset0:80 offset1:88
	ds_write2st64_b32 v28, v58, v59 offset0:96 offset1:104
	ds_write2st64_b32 v28, v60, v61 offset0:112 offset1:120
	s_cmp_gt_i32 s82, 0
	v_add_u32_e32 v6, 0x400, v0
	v_ashrrev_i32_e32 v42, 11, v6
	v_add_u32_e32 v4, s0, v42
	v_and_b32_e32 v6, 0x7ff, v6
	v_lshlrev_b32_e32 v22, 2, v6
	v_add_u32_e32 v4, s0, v41
	v_add_u32_e32 v4, 0x800, v0
	v_ashrrev_i32_e32 v40, 11, v4
	v_add_u32_e32 v4, s0, v40
	v_add_u32_e32 v4, s0, v39
	v_add_u32_e32 v6, 0xc00, v0
	v_ashrrev_i32_e32 v38, 11, v6
	v_add_u32_e32 v4, s0, v38
	v_and_b32_e32 v6, 0x7ff, v6
	v_lshlrev_b32_e32 v16, 2, v6
	v_add_u32_e32 v4, s0, v37
	v_add_u32_e32 v4, 0x1000, v0
	v_ashrrev_i32_e32 v36, 11, v4
	v_add_u32_e32 v4, s0, v36
	v_add_u32_e32 v4, s0, v35
	v_add_u32_e32 v6, 0x1400, v0
	v_ashrrev_i32_e32 v34, 11, v6
	v_add_u32_e32 v4, s0, v34
	v_and_b32_e32 v6, 0x7ff, v6
	v_lshlrev_b32_e32 v10, 2, v6
	v_add_u32_e32 v4, s0, v33
	v_add_u32_e32 v4, 0x1800, v0
	v_ashrrev_i32_e32 v32, 11, v4
	v_add_u32_e32 v4, s0, v32
	v_add_u32_e32 v6, 0x1a00, v0
	v_ashrrev_i32_e32 v31, 11, v6
	v_add_u32_e32 v4, s0, v31
	v_and_b32_e32 v6, 0x7ff, v6
	v_lshlrev_b32_e32 v6, 2, v6
	v_add_u32_e32 v7, 0x1e00, v0
	v_ashrrev_i32_e32 v29, 11, v7
	v_add_u32_e32 v4, 0x1c00, v0
	v_ashrrev_i32_e32 v30, 11, v4
	v_add_u32_e32 v5, s0, v30
	v_and_b32_e32 v4, 0x7ff, v4
	v_lshlrev_b32_e32 v4, 2, v4
	v_mov_b32_e32 v5, v169
	v_add_u32_e32 v9, s0, v29
	v_and_b32_e32 v2, 0x7ff, v7
	v_lshlrev_b32_e32 v2, 2, v2
	v_mov_b32_e32 v3, v169
	s_mov_b64 s[2:3], -1
	s_cselect_b64 s[0:1], -1, 0
	s_cmp_lt_i32 s82, 1
	s_cbranch_scc1 .LBB0_1595
	s_movk_i32 s2, 0x800
	v_cmp_gt_i32_e32 vcc, s2, v0
	s_and_saveexec_b64 s[2:3], vcc
	s_cbranch_execz .LBB0_1594
	v_max_i32_e32 v3, 0x600, v0
	v_sub_u32_e32 v3, v3, v0
	v_add_u32_e32 v3, 0x1ff, v3
	s_movk_i32 s4, 0x1ff
	v_cmp_lt_u32_e32 vcc, s4, v3
	s_mov_b64 s[6:7], -1
	v_mov_b32_e32 v26, v0
	s_and_saveexec_b64 s[4:5], vcc
	s_cbranch_execz .LBB0_1591
	v_lshrrev_b32_e32 v3, 9, v3
	v_readlane_b32 s36, v253, 32
	v_readlane_b32 s48, v253, 44
	v_add_u32_e32 v7, -1, v3
	v_readlane_b32 s49, v253, 45
	s_add_u32 s6, s48, s10
	v_lshrrev_b32_e32 v5, 1, v7
	s_addc_u32 s7, s49, s11
	v_add_u32_e32 v5, 1, v5
	v_cmp_lt_u32_e32 vcc, 13, v7
	v_mov_b32_e32 v11, 0
	v_mov_b64_e32 v[26:27], v[0:1]
	v_readlane_b32 s37, v253, 33
	v_readlane_b32 s38, v253, 34
	v_readlane_b32 s39, v253, 35
	v_readlane_b32 s40, v253, 36
	v_readlane_b32 s41, v253, 37
	v_readlane_b32 s42, v253, 38
	v_readlane_b32 s43, v253, 39
	v_readlane_b32 s44, v253, 40
	v_readlane_b32 s45, v253, 41
	v_readlane_b32 s46, v253, 42
	v_readlane_b32 s47, v253, 43
	v_readlane_b32 s50, v253, 46
	v_readlane_b32 s51, v253, 47
	s_and_saveexec_b64 s[8:9], vcc
	s_cbranch_execz .LBB0_1587
	s_add_i32 s12, 0, 0x8000
	v_and_b32_e32 v7, -8, v5
	v_lshl_add_u32 v9, v0, 2, s12
	s_mov_b32 s15, 0
	s_mov_b64 s[12:13], 0
	v_mov_b64_e32 v[26:27], v[0:1]

.LBB0_1595:
	s_andn2_b64 vcc, exec, s[2:3]
	s_cbranch_vccnz .LBB0_1597
	v_readlane_b32 s46, v253, 10
	v_readlane_b32 s47, v253, 11
	v_add_u32_e32 v1, 0x1000, v28
	v_add_u32_e32 v2, 0x2000, v28
	v_add_u32_e32 v3, 0x3000, v28
	v_add_u32_e32 v24, 0x10000, v28
	s_add_u32 s6, s46, s10
	s_addc_u32 s7, s47, s11
	s_add_i32 s4, s82, 1
	s_ashr_i32 s5, s4, 31
	s_lshl_b64 s[2:3], s[4:5], 13
	s_add_u32 s2, s6, s2
	s_addc_u32 s3, s7, s3
	s_mul_i32 s5, s4, 0x30000
	s_add_u32 s36, s18, 0x100000
	s_addc_u32 s37, s19, 0
	s_add_u32 s36, s36, s5
	s_addc_u32 s37, s37, 0
	s_add_u32 s38, s36, 0xc000
	s_addc_u32 s39, s37, 0
	s_add_u32 s40, s36, 0x18000
	s_addc_u32 s41, s37, 0
	s_add_u32 s42, s36, 0x24000
	s_addc_u32 s43, s37, 0
	global_load_dword v4, v28, s[2:3]
	global_load_dword v5, v28, s[2:3] offset:2048
	global_load_dword v6, v1, s[2:3]
	global_load_dword v7, v1, s[2:3] offset:2048
	global_load_dword v8, v2, s[36:37]
	global_load_dword v32, v28, s[36:37]
	global_load_dword v9, v2, s[36:37] offset:2048
	global_load_dword v33, v28, s[36:37] offset:2048
	global_load_dword v10, v3, s[36:37]
	global_load_dword v34, v1, s[36:37]
	global_load_dword v11, v3, s[36:37] offset:2048
	global_load_dword v35, v1, s[36:37] offset:2048
	global_load_dword v12, v2, s[38:39]
	global_load_dword v36, v28, s[38:39]
	global_load_dword v13, v2, s[38:39] offset:2048
	global_load_dword v37, v28, s[38:39] offset:2048
	global_load_dword v14, v3, s[38:39]
	global_load_dword v38, v1, s[38:39]
	global_load_dword v15, v3, s[38:39] offset:2048
	global_load_dword v39, v1, s[38:39] offset:2048
	global_load_dword v16, v2, s[40:41]
	global_load_dword v40, v28, s[40:41]
	global_load_dword v17, v2, s[40:41] offset:2048
	global_load_dword v41, v28, s[40:41] offset:2048
	global_load_dword v18, v3, s[40:41]
	global_load_dword v42, v1, s[40:41]
	global_load_dword v19, v3, s[40:41] offset:2048
	global_load_dword v43, v1, s[40:41] offset:2048
	global_load_dword v20, v2, s[42:43]
	global_load_dword v44, v28, s[42:43]
	global_load_dword v21, v2, s[42:43] offset:2048
	global_load_dword v45, v28, s[42:43] offset:2048
	global_load_dword v22, v3, s[42:43]
	global_load_dword v46, v1, s[42:43]
	global_load_dword v23, v3, s[42:43] offset:2048
	global_load_dword v47, v1, s[42:43] offset:2048
	s_waitcnt vmcnt(0)
	v_add_f32_e32 v8, 1.0, v8
	v_add_f32_e32 v9, 1.0, v9
	v_add_f32_e32 v10, 1.0, v10
	v_add_f32_e32 v11, 1.0, v11
	v_add_f32_e32 v12, 1.0, v12
	v_add_f32_e32 v13, 1.0, v13
	v_add_f32_e32 v14, 1.0, v14
	v_add_f32_e32 v15, 1.0, v15
	v_add_f32_e32 v16, 1.0, v16
	v_add_f32_e32 v17, 1.0, v17
	v_add_f32_e32 v18, 1.0, v18
	v_add_f32_e32 v19, 1.0, v19
	v_add_f32_e32 v20, 1.0, v20
	v_add_f32_e32 v21, 1.0, v21
	v_add_f32_e32 v22, 1.0, v22
	v_add_f32_e32 v23, 1.0, v23
	v_mul_f32_e32 v8, v4, v8
	v_mul_f32_e32 v9, v5, v9
	v_mul_f32_e32 v10, v6, v10
	v_mul_f32_e32 v11, v7, v11
	v_mul_f32_e32 v12, v4, v12
	v_mul_f32_e32 v13, v5, v13
	v_mul_f32_e32 v14, v6, v14
	v_mul_f32_e32 v15, v7, v15
	v_mul_f32_e32 v16, v4, v16
	v_mul_f32_e32 v17, v5, v17
	v_mul_f32_e32 v18, v6, v18
	v_mul_f32_e32 v19, v7, v19
	v_mul_f32_e32 v20, v4, v20
	v_mul_f32_e32 v21, v5, v21
	v_mul_f32_e32 v22, v6, v22
	v_mul_f32_e32 v23, v7, v23
	ds_write2st64_b32 v28, v8, v9 offset0:128 offset1:136
	ds_write2st64_b32 v24, v32, v33 offset1:8
	ds_write2st64_b32 v28, v10, v11 offset0:144 offset1:152
	ds_write2st64_b32 v24, v34, v35 offset0:16 offset1:24
	ds_write2st64_b32 v28, v12, v13 offset0:160 offset1:168
	ds_write2st64_b32 v24, v36, v37 offset0:32 offset1:40
	ds_write2st64_b32 v28, v14, v15 offset0:176 offset1:184
	ds_write2st64_b32 v24, v38, v39 offset0:48 offset1:56
	ds_write2st64_b32 v28, v16, v17 offset0:192 offset1:200
	ds_write2st64_b32 v24, v40, v41 offset0:64 offset1:72
	ds_write2st64_b32 v28, v18, v19 offset0:208 offset1:216
	ds_write2st64_b32 v24, v42, v43 offset0:80 offset1:88
	ds_write2st64_b32 v28, v20, v21 offset0:224 offset1:232
	ds_write2st64_b32 v24, v44, v45 offset0:96 offset1:104
	ds_write2st64_b32 v28, v22, v23 offset0:240 offset1:248
	ds_write2st64_b32 v24, v46, v47 offset0:112 offset1:120
